# final phase: software-pipelined row loop (next row's x/slot/gate loads prefetched one row ahead)
# speedup vs baseline: 1.0104x; 1.0067x over previous
.LBB0_4626:
	s_or_b64 exec, exec, s[0:1]
	s_ashr_i32 s0, s3, 6
	s_add_i32 s4, s0, s78
	s_cmpk_gt_i32 s4, 0x3fff
	s_waitcnt lgkmcnt(0)
	s_barrier
	s_cbranch_scc1 .LBB0_4629
	v_and_b32_e32 v2, 63, v0
	v_lshlrev_b32_e32 v4, 4, v2
	v_lshlrev_b32_e32 v0, 2, v2
	v_mov_b32_e32 v5, 0
	v_xor_b32_e32 v56, 64, v0
	v_xor_b32_e32 v57, 0x80, v0
	v_or_b32_e32 v0, 0x1000, v4
	v_mov_b32_e32 v1, v5
	v_lshl_add_u64 v[8:9], s[70:71], 0, v[0:1]
	v_or_b32_e32 v0, 0x1400, v4
	s_add_u32 s10, s74, 0x3b400000
	v_lshl_add_u64 v[10:11], s[70:71], 0, v[0:1]
	v_or_b32_e32 v0, 0x1800, v4
	s_addc_u32 s11, s75, 0
	v_lshl_add_u64 v[12:13], s[70:71], 0, v[0:1]
	v_or_b32_e32 v0, 0x1c00, v4
	s_add_u32 s12, s74, 0x3b500000
	v_lshl_add_u64 v[14:15], s[70:71], 0, v[0:1]
	v_lshlrev_b32_e32 v0, 3, v2
	s_addc_u32 s13, s75, 0
	v_lshl_add_u64 v[2:3], s[74:75], 0, v[0:1]
	s_mov_b64 s[2:3], 0x26c00000
	s_lshl_b32 s1, s96, 4
	s_lshl_b32 s0, s0, 1
	s_ashr_i32 s5, s4, 31
	v_lshl_add_u64 v[16:17], v[2:3], 0, s[2:3]
	s_add_i32 s2, s1, s0
	s_lshl_b32 s14, s76, 4
	s_lshl_b64 s[0:1], s[4:5], 12
	s_add_u32 s0, s74, s0
	s_addc_u32 s1, s75, s1
	v_lshl_add_u64 v[0:1], s[0:1], 0, v[0:1]
	s_mov_b64 s[0:1], 0xe400000
	s_ashr_i32 s95, s94, 31
	v_lshl_add_u64 v[18:19], v[0:1], 0, s[0:1]
	s_lshl_b64 s[6:7], s[94:95], 12
	s_lshl_b64 s[0:1], s[4:5], 13
	s_add_u32 s0, s72, s0
	s_addc_u32 s1, s73, s1
	v_lshl_add_u64 v[0:1], s[0:1], 0, v[4:5]
	s_mov_b64 s[0:1], 0x1000
	v_lshl_add_u64 v[6:7], s[70:71], 0, v[4:5]
	v_lshl_add_u64 v[20:21], v[0:1], 0, s[0:1]
	s_lshl_b64 s[8:9], s[94:95], 13
	s_add_i32 s5, 0, 0x20080
	v_mov_b32_e32 v4, 0x358637bd
	s_mov_b32 s15, 0xf800000
	v_mov_b32_e32 v58, 0x260
	global_load_dwordx4 v[130:133], v[6:7], off
	global_load_dwordx4 v[134:137], v[6:7], off offset:1024
	global_load_dwordx4 v[138:141], v[6:7], off offset:2048
	global_load_dwordx4 v[142:145], v[6:7], off offset:3072
	global_load_dwordx4 v[146:149], v[8:9], off
	global_load_dwordx4 v[150:153], v[10:11], off
	global_load_dwordx4 v[154:157], v[12:13], off
	global_load_dwordx4 v[158:161], v[14:15], off
	s_waitcnt vmcnt(0)
	s_ashr_i32 s3, s2, 31
	s_lshl_b64 s[0:1], s[2:3], 2
	s_add_u32 s16, s10, s0
	s_addc_u32 s17, s11, s1
	global_load_dwordx2 v[162:163], v[18:19], off offset:2560
	global_load_dwordx2 v[164:165], v[18:19], off offset:3072
	global_load_dwordx2 v[166:167], v[18:19], off offset:3584
	global_load_dwordx2 v[168:169], v[18:19], off offset:1024
	global_load_dwordx2 v[170:171], v[18:19], off offset:1536
	global_load_dwordx2 v[172:173], v[18:19], off offset:2048
	global_load_dwordx2 v[174:175], v[18:19], off
	global_load_dwordx2 v[176:177], v[18:19], off offset:512
	global_load_dwordx2 v[178:179], v5, s[16:17]
	s_add_i32 s18, s2, 1
	s_ashr_i32 s19, s18, 31
	s_add_u32 s0, s12, s0
	s_addc_u32 s1, s13, s1
	global_load_dword v180, v5, s[0:1]
	s_lshl_b64 s[16:17], s[18:19], 2
	s_add_u32 s0, s12, s16
	s_addc_u32 s1, s13, s17
	global_load_dword v181, v5, s[0:1]
	s_add_i32 s4, s4, s94
	s_add_i32 s2, s2, s14
	v_lshl_add_u64 v[18:19], v[18:19], 0, s[6:7]
	s_waitcnt vmcnt(0)
.LBB0_4628:
	v_mov_b64_e32 v[22:23], v[162:163]
	v_mov_b64_e32 v[24:25], v[164:165]
	v_mov_b64_e32 v[30:31], v[166:167]
	v_mov_b64_e32 v[42:43], v[168:169]
	v_mov_b64_e32 v[46:47], v[170:171]
	v_mov_b64_e32 v[26:27], v[172:173]
	v_mov_b64_e32 v[52:53], v[174:175]
	v_mov_b64_e32 v[34:35], v[176:177]
	v_mov_b64_e32 v[60:61], v[178:179]
	v_mov_b64_e32 v[28:29], v[180:181]
	s_ashr_i32 s3, s2, 31
	s_lshl_b64 s[0:1], s[2:3], 2
	s_add_u32 s16, s10, s0
	s_addc_u32 s17, s11, s1
	global_load_dwordx2 v[162:163], v[18:19], off offset:2560
	global_load_dwordx2 v[164:165], v[18:19], off offset:3072
	global_load_dwordx2 v[166:167], v[18:19], off offset:3584
	global_load_dwordx2 v[168:169], v[18:19], off offset:1024
	global_load_dwordx2 v[170:171], v[18:19], off offset:1536
	global_load_dwordx2 v[172:173], v[18:19], off offset:2048
	global_load_dwordx2 v[174:175], v[18:19], off
	global_load_dwordx2 v[176:177], v[18:19], off offset:512
	global_load_dwordx2 v[178:179], v5, s[16:17]
	s_add_i32 s18, s2, 1
	s_ashr_i32 s19, s18, 31
	s_add_u32 s0, s12, s0
	s_addc_u32 s1, s13, s1
	global_load_dword v180, v5, s[0:1]
	s_lshl_b64 s[16:17], s[18:19], 2
	s_add_u32 s0, s12, s16
	s_addc_u32 s1, s13, s17
	global_load_dword v181, v5, s[0:1]
	s_add_i32 s4, s4, s94
	s_add_i32 s2, s2, s14
	v_lshl_add_u64 v[18:19], v[18:19], 0, s[6:7]
	s_sub_i32 s3, s4, s94
	s_cmpk_lt_i32 s3, 0x4000
	v_and_b32_e32 v59, 0xffff0000, v22
	v_lshlrev_b32_e32 v36, 16, v24
	v_and_b32_e32 v114, 0xffff0000, v24
	v_lshlrev_b32_e32 v38, 16, v25
	v_and_b32_e32 v126, 0xffff0000, v25
	v_lshlrev_b32_e32 v48, 16, v27
	v_and_b32_e32 v49, 0xffff0000, v27
	v_lshlrev_b32_e32 v62, 16, v26
	v_and_b32_e32 v63, 0xffff0000, v26
	v_lshlrev_b32_e32 v26, 16, v23
	v_and_b32_e32 v27, 0xffff0000, v23
	v_lshrrev_b32_e32 v23, 18, v60
	v_lshrrev_b32_e32 v24, 18, v61
	v_and_b32_e32 v23, 0x3ffc, v23
	v_and_b32_e32 v24, 0x3ffc, v24
	v_add_u32_e32 v23, s5, v23
	v_add_u32_e32 v24, s5, v24
	ds_read_b32 v23, v23
	ds_read_b32 v37, v24
	v_lshlrev_b32_e32 v127, 16, v30
	v_and_b32_e32 v25, 0xffff0000, v30
	v_and_b32_e32 v30, 0xfffff, v60
	v_and_b32_e32 v32, 0xfffff, v61
	s_waitcnt lgkmcnt(1)
	v_add_u32_e32 v64, v23, v30
	s_waitcnt lgkmcnt(0)
	v_add_u32_e32 v66, v37, v32
	v_ashrrev_i32_e32 v65, 31, v64
	v_ashrrev_i32_e32 v67, 31, v66
	v_lshlrev_b64 v[64:65], 12, v[64:65]
	v_lshlrev_b64 v[66:67], 12, v[66:67]
	v_lshl_add_u64 v[64:65], v[16:17], 0, v[64:65]
	v_lshl_add_u64 v[66:67], v[16:17], 0, v[66:67]
	global_load_dwordx2 v[68:69], v[66:67], off offset:512
	global_load_dwordx2 v[70:71], v[64:65], off offset:512
	global_load_dwordx2 v[72:73], v[66:67], off offset:2048
	global_load_dwordx2 v[74:75], v[64:65], off offset:2048
	global_load_dwordx2 v[76:77], v[66:67], off offset:2560
	global_load_dwordx2 v[78:79], v[64:65], off offset:2560
	global_load_dwordx2 v[80:81], v[66:67], off offset:3072
	global_load_dwordx2 v[82:83], v[64:65], off offset:3072
	global_load_dwordx2 v[84:85], v[64:65], off offset:3584
	global_load_dwordx2 v[86:87], v[66:67], off offset:3584
	global_load_dwordx2 v[88:89], v[64:65], off offset:1024
	global_load_dwordx2 v[90:91], v[66:67], off offset:1024
	global_load_dwordx2 v[92:93], v[64:65], off offset:1536
	global_load_dwordx2 v[94:95], v[66:67], off offset:1536
	global_load_dwordx2 v[96:97], v[64:65], off
	s_nop 0
	global_load_dwordx2 v[64:65], v[66:67], off
	v_mov_b32_e32 v24, v29
	v_lshlrev_b32_e32 v33, 16, v31
	v_and_b32_e32 v31, 0xffff0000, v31
	v_lshlrev_b32_e32 v50, 16, v52
	v_and_b32_e32 v51, 0xffff0000, v52
	v_lshlrev_b32_e32 v52, 16, v53
	v_and_b32_e32 v53, 0xffff0000, v53
	v_lshlrev_b32_e32 v54, 16, v34
	v_and_b32_e32 v55, 0xffff0000, v34
	v_lshlrev_b32_e32 v34, 16, v35
	v_and_b32_e32 v35, 0xffff0000, v35
	v_lshlrev_b32_e32 v22, 16, v22
	v_lshlrev_b32_e32 v41, 16, v43
	v_lshlrev_b32_e32 v40, 16, v42
	v_and_b32_e32 v43, 0xffff0000, v43
	v_and_b32_e32 v42, 0xffff0000, v42
	v_lshlrev_b32_e32 v45, 16, v47
	v_lshlrev_b32_e32 v44, 16, v46
	v_and_b32_e32 v47, 0xffff0000, v47
	v_and_b32_e32 v46, 0xffff0000, v46
	v_mov_b32_e32 v61, v28
	s_waitcnt vmcnt(15)
	v_lshlrev_b32_e32 v67, 16, v68
	s_waitcnt vmcnt(14)
	v_lshlrev_b32_e32 v66, 16, v70
	v_and_b32_e32 v99, 0xffff0000, v68
	v_and_b32_e32 v98, 0xffff0000, v70
	v_lshlrev_b32_e32 v101, 16, v69
	v_lshlrev_b32_e32 v100, 16, v71
	v_and_b32_e32 v69, 0xffff0000, v69
	v_and_b32_e32 v68, 0xffff0000, v71
	s_waitcnt vmcnt(13)
	v_lshlrev_b32_e32 v71, 16, v72
	s_waitcnt vmcnt(12)
	v_lshlrev_b32_e32 v70, 16, v74
	v_and_b32_e32 v103, 0xffff0000, v72
	v_and_b32_e32 v102, 0xffff0000, v74
	s_waitcnt vmcnt(10)
	v_lshlrev_b32_e32 v104, 16, v78
	v_and_b32_e32 v106, 0xffff0000, v78
	s_waitcnt vmcnt(8)
	v_lshlrev_b32_e32 v78, 16, v82
	v_and_b32_e32 v110, 0xffff0000, v82
	s_waitcnt vmcnt(6)
	v_lshlrev_b32_e32 v115, 16, v86
	v_and_b32_e32 v32, 0xffff0000, v86
	v_lshlrev_b32_e32 v39, 16, v87
	v_and_b32_e32 v82, 0xffff0000, v87
	s_waitcnt vmcnt(4)
	v_lshlrev_b32_e32 v87, 16, v91
	v_lshlrev_b32_e32 v86, 16, v90
	v_and_b32_e32 v91, 0xffff0000, v91
	v_and_b32_e32 v90, 0xffff0000, v90
	s_waitcnt vmcnt(2)
	v_lshlrev_b32_e32 v119, 16, v95
	v_lshlrev_b32_e32 v118, 16, v94
	v_and_b32_e32 v95, 0xffff0000, v95
	v_and_b32_e32 v94, 0xffff0000, v94
	v_and_b32_e32 v121, 0xffff0000, v75
	v_lshlrev_b32_e32 v120, 16, v75
	v_and_b32_e32 v75, 0xffff0000, v73
	v_lshlrev_b32_e32 v74, 16, v73
	s_waitcnt vmcnt(1)
	v_and_b32_e32 v73, 0xffff0000, v96
	v_lshlrev_b32_e32 v72, 16, v96
	v_and_b32_e32 v125, 0xffff0000, v97
	v_lshlrev_b32_e32 v124, 16, v97
	s_waitcnt vmcnt(0)
	v_and_b32_e32 v97, 0xffff0000, v65
	v_lshlrev_b32_e32 v96, 16, v65
	v_lshlrev_b32_e32 v105, 16, v76
	v_and_b32_e32 v107, 0xffff0000, v76
	v_lshlrev_b32_e32 v108, 16, v79
	v_and_b32_e32 v76, 0xffff0000, v79
	v_lshlrev_b32_e32 v79, 16, v80
	v_and_b32_e32 v111, 0xffff0000, v80
	v_lshlrev_b32_e32 v113, 16, v81
	v_lshlrev_b32_e32 v112, 16, v83
	v_and_b32_e32 v81, 0xffff0000, v81
	v_and_b32_e32 v80, 0xffff0000, v83
	v_lshlrev_b32_e32 v83, 16, v84
	v_and_b32_e32 v23, 0xffff0000, v84
	v_lshlrev_b32_e32 v37, 16, v85
	v_and_b32_e32 v60, 0xffff0000, v85
	v_lshlrev_b32_e32 v85, 16, v89
	v_lshlrev_b32_e32 v84, 16, v88
	v_and_b32_e32 v89, 0xffff0000, v89
	v_and_b32_e32 v88, 0xffff0000, v88
	v_lshlrev_b32_e32 v117, 16, v93
	v_lshlrev_b32_e32 v116, 16, v92
	v_and_b32_e32 v93, 0xffff0000, v93
	v_and_b32_e32 v92, 0xffff0000, v92
	v_and_b32_e32 v123, 0xffff0000, v64
	v_lshlrev_b32_e32 v122, 16, v64
	v_pk_mul_f32 v[64:65], v[28:29], v[66:67]
	v_pk_mul_f32 v[66:67], v[28:29], v[98:99]
	v_pk_mul_f32 v[98:99], v[28:29], v[100:101]
	v_pk_mul_f32 v[68:69], v[28:29], v[68:69]
	v_pk_mul_f32 v[86:87], v[24:25], v[86:87] op_sel_hi:[0,1]
	v_pk_mul_f32 v[90:91], v[24:25], v[90:91] op_sel_hi:[0,1]
	v_pk_mul_f32 v[94:95], v[24:25], v[94:95] op_sel_hi:[0,1]
	v_pk_mul_f32 v[96:97], v[24:25], v[96:97] op_sel_hi:[0,1]
	v_lshlrev_b32_e32 v109, 16, v77
	v_pk_mul_f32 v[100:101], v[28:29], v[102:103]
	v_pk_mul_f32 v[102:103], v[28:29], v[106:107]
	v_pk_mul_f32 v[80:81], v[28:29], v[80:81]
	v_mul_f32_e32 v30, v29, v105
	v_pk_mul_f32 v[118:119], v[24:25], v[118:119] op_sel_hi:[0,1]
	v_pk_mul_f32 v[74:75], v[24:25], v[74:75] op_sel_hi:[0,1]
	v_pk_mul_f32 v[122:123], v[24:25], v[122:123] op_sel_hi:[0,1]
	v_mul_f32_e32 v24, v29, v79
	v_pk_fma_f32 v[84:85], v[28:29], v[84:85], v[86:87] op_sel_hi:[0,1,1]
	v_pk_fma_f32 v[86:87], v[28:29], v[88:89], v[90:91] op_sel_hi:[0,1,1]
	v_pk_fma_f32 v[90:91], v[28:29], v[92:93], v[94:95] op_sel_hi:[0,1,1]
	v_pk_fma_f32 v[92:93], v[28:29], v[124:125], v[96:97] op_sel_hi:[0,1,1]
	v_mov_b32_e32 v96, v64
	v_mov_b32_e32 v97, v66
	v_mov_b32_e32 v66, v65
	v_mov_b32_e32 v64, v98
	v_mov_b32_e32 v65, v68
	v_mov_b32_e32 v68, v99
	v_and_b32_e32 v77, 0xffff0000, v77
	v_pk_mul_f32 v[70:71], v[28:29], v[70:71]
	v_pk_mul_f32 v[106:107], v[28:29], v[108:109]
	v_pk_mul_f32 v[108:109], v[28:29], v[110:111]
	v_mul_f32_e32 v110, v28, v37
	v_mul_f32_e32 v37, v29, v39
	v_mul_f32_e32 v39, v29, v82
	v_add_f32_e32 v82, v102, v103
	v_add_f32_e32 v103, v80, v81
	v_pk_fma_f32 v[80:81], v[28:29], v[104:105], v[30:31] op_sel_hi:[1,1,0]
	v_pk_fma_f32 v[72:73], v[28:29], v[72:73], v[122:123] op_sel_hi:[0,1,1]
	v_pk_fma_f32 v[78:79], v[28:29], v[78:79], v[24:25] op_sel_hi:[1,1,0]
	v_pk_add_f32 v[66:67], v[96:97], v[66:67]
	v_pk_add_f32 v[64:65], v[64:65], v[68:69]
	v_pk_mul_f32 v[76:77], v[28:29], v[76:77]
	v_mul_f32_e32 v111, v29, v32
	v_mul_f32_e32 v32, v29, v113
	v_add_f32_e32 v102, v108, v109
	v_mov_b32_e32 v98, v70
	v_mov_b32_e32 v99, v100
	v_mov_b32_e32 v100, v71
	v_mov_b32_e32 v81, v28
	v_pk_add_f32 v[50:51], v[72:73], v[50:51]
	v_pk_add_f32 v[52:53], v[92:93], v[52:53]
	v_mov_b32_e32 v79, v110
	v_pk_add_f32 v[54:55], v[66:67], v[54:55]
	v_pk_add_f32 v[34:35], v[64:65], v[34:35]
	v_mul_f32_e32 v60, v28, v60
	v_pk_fma_f32 v[88:89], v[28:29], v[116:117], v[118:119] op_sel_hi:[0,1,1]
	v_pk_fma_f32 v[74:75], v[28:29], v[120:121], v[74:75] op_sel_hi:[0,1,1]
	v_pk_fma_f32 v[94:95], v[28:29], v[112:113], v[32:33] op_sel_hi:[1,1,0]
	v_mov_b32_e32 v70, v106
	v_mov_b32_e32 v71, v76
	v_mov_b32_e32 v76, v107
	v_add_f32_e32 v102, v102, v114
	v_pk_add_f32 v[42:43], v[86:87], v[42:43]
	v_pk_add_f32 v[46:47], v[90:91], v[46:47]
	v_pk_add_f32 v[68:69], v[98:99], v[100:101]
	v_pk_add_f32 v[72:73], v[80:81], v[22:23]
	v_pk_mul_f32 v[22:23], v[80:81], v[22:23]
	v_pk_add_f32 v[36:37], v[78:79], v[36:37]
	v_mov_b32_e32 v78, v51
	v_mov_b32_e32 v80, v53
	v_mov_b32_e32 v79, v55
	v_mov_b32_e32 v81, v35
	v_add_f32_e32 v103, v103, v126
	v_pk_add_f32 v[40:41], v[84:85], v[40:41]
	v_pk_add_f32 v[44:45], v[88:89], v[44:45]
	v_pk_add_f32 v[48:49], v[74:75], v[48:49]
	v_mov_b32_e32 v95, v60
	v_pk_add_f32 v[70:71], v[70:71], v[76:77]
	v_pk_mul_f32 v[74:75], v[42:43], v[42:43]
	v_pk_mul_f32 v[76:77], v[46:47], v[46:47]
	v_mul_f32_e32 v28, v102, v102
	v_mov_b32_e32 v66, v50
	v_mov_b32_e32 v64, v52
	v_pk_add_f32 v[62:63], v[68:69], v[62:63]
	v_mov_b32_e32 v22, v72
	v_mov_b32_e32 v110, v72
	v_mov_b32_e32 v67, v54
	v_mov_b32_e32 v65, v34
	v_pk_mul_f32 v[78:79], v[78:79], v[78:79]
	v_pk_mul_f32 v[80:81], v[80:81], v[80:81]
	v_add_f32_e32 v59, v82, v59
	v_mul_f32_e32 v60, v103, v103
	v_pk_add_f32 v[38:39], v[94:95], v[38:39]
	v_pk_add_f32 v[26:27], v[70:71], v[26:27]
	v_pk_fma_f32 v[68:69], v[40:41], v[40:41], v[74:75]
	v_pk_fma_f32 v[70:71], v[44:45], v[44:45], v[76:77]
	v_pk_mul_f32 v[76:77], v[72:73], v[72:73]
	v_pk_fma_f32 v[84:85], v[36:37], v[36:37], v[28:29]
	v_mov_b32_e32 v28, v63
	v_mov_b32_e32 v114, v63
	v_pk_add_f32 v[22:23], v[22:23], v[110:111]
	v_pk_fma_f32 v[66:67], v[66:67], v[66:67], v[78:79]
	v_pk_fma_f32 v[64:65], v[64:65], v[64:65], v[80:81]
	v_mul_f32_e32 v24, v59, v59
	v_pk_fma_f32 v[86:87], v[38:39], v[38:39], v[60:61]
	v_mov_b32_e32 v60, v62
	v_mov_b32_e32 v82, v62
	v_pk_mul_f32 v[88:89], v[26:27], v[26:27]
	v_pk_add_f32 v[68:69], v[68:69], v[68:69] op_sel:[0,1] op_sel_hi:[1,0]
	v_pk_mul_f32 v[28:29], v[28:29], v[114:115]
	v_mov_b32_e32 v77, v23
	v_pk_add_f32 v[64:65], v[66:67], v[64:65]
	v_mul_f32_e32 v30, v49, v49
	v_pk_mul_f32 v[90:91], v[60:61], v[82:83]
	v_pk_fma_f32 v[60:61], v[60:61], v[82:83], v[28:29]
	v_mov_b32_e32 v69, v29
	v_mov_b32_e32 v22, v88
	v_pk_add_f32 v[28:29], v[76:77], v[24:25]
	v_mov_b32_e32 v24, v89
	v_pk_add_f32 v[64:65], v[64:65], v[64:65] op_sel:[0,1] op_sel_hi:[1,0]
	v_pk_fma_f32 v[74:75], v[48:49], v[48:49], v[30:31] op_sel_hi:[1,1,0]
	v_pk_add_f32 v[70:71], v[70:71], v[70:71] op_sel:[0,1] op_sel_hi:[1,0]
	v_pk_add_f32 v[22:23], v[22:23], v[24:25]
	v_mov_b32_e32 v65, v91
	v_mov_b32_e32 v32, v36
	v_mov_b32_e32 v30, v38
	v_mov_b32_e32 v75, v127
	v_mov_b32_e32 v71, v127
	v_pk_add_f32 v[24:25], v[28:29], v[22:23]
	v_pk_mul_f32 v[22:23], v[28:29], v[22:23]
	v_pk_add_f32 v[64:65], v[64:65], v[68:69]
	v_pk_add_f32 v[32:33], v[36:37], v[32:33]
	v_pk_add_f32 v[30:31], v[38:39], v[30:31]
	v_pk_add_f32 v[60:61], v[60:61], v[74:75]
	v_mov_b32_e32 v25, v23
	v_pk_add_f32 v[22:23], v[64:65], v[70:71]
	v_pk_mul_f32 v[92:93], v[32:33], v[32:33]
	v_pk_mul_f32 v[94:95], v[30:31], v[30:31]
	v_pk_add_f32 v[64:65], v[22:23], v[60:61]
	v_pk_mul_f32 v[60:61], v[22:23], v[60:61]
	v_mov_b32_e32 v85, v93
	v_mov_b32_e32 v87, v95
	v_mov_b32_e32 v65, v61
	v_pk_add_f32 v[66:67], v[84:85], v[86:87]
	v_pk_add_f32 v[24:25], v[64:65], v[24:25]
	v_mov_b32_e32 v73, v59
	v_pk_add_f32 v[24:25], v[24:25], v[66:67]
	v_mov_b32_e32 v37, v102
	v_add_f32_e32 v22, v24, v25
	v_mov_b32_e32 v39, v103
	s_nop 0
	v_add_f32_dpp v22, v22, v22 quad_perm:[1,0,3,2] row_mask:0xf bank_mask:0xf bound_ctrl:1
	s_nop 1
	v_add_f32_dpp v22, v22, v22 quad_perm:[2,3,0,1] row_mask:0xf bank_mask:0xf bound_ctrl:1
	s_nop 1
	v_add_f32_dpp v22, v22, v22 row_ror:4 row_mask:0xf bank_mask:0xf bound_ctrl:1
	s_nop 1
	v_add_f32_dpp v22, v22, v22 row_ror:8 row_mask:0xf bank_mask:0xf bound_ctrl:1
	ds_bpermute_b32 v24, v56, v22
	s_waitcnt lgkmcnt(0)
	v_add_f32_e32 v22, v22, v24
	ds_bpermute_b32 v24, v57, v22
	s_waitcnt lgkmcnt(0)
	v_add_f32_e32 v22, v22, v24
	v_fmamk_f32 v22, v22, 0x3a000000, v4
	v_mul_f32_e32 v24, 0x4f800000, v22
	v_cmp_gt_f32_e32 vcc, s15, v22
	s_nop 1
	v_cndmask_b32_e32 v22, v22, v24, vcc
	v_sqrt_f32_e32 v24, v22
	s_nop 0
	v_add_u32_e32 v25, -1, v24
	v_add_u32_e32 v28, 1, v24
	v_fma_f32 v30, -v25, v24, v22
	v_fma_f32 v32, -v28, v24, v22
	v_cmp_ge_f32_e64 s[0:1], 0, v30
	s_nop 1
	v_cndmask_b32_e64 v24, v24, v25, s[0:1]
	v_cmp_lt_f32_e64 s[0:1], 0, v32
	s_nop 1
	v_cndmask_b32_e64 v24, v24, v28, s[0:1]
	v_mul_f32_e32 v25, 0x37800000, v24
	v_cndmask_b32_e32 v24, v24, v25, vcc
	v_cmp_class_f32_e32 vcc, v22, v58
	s_nop 1
	v_cndmask_b32_e32 v22, v24, v22, vcc
	v_div_scale_f32 v24, s[0:1], v22, v22, 1.0
	v_rcp_f32_e32 v28, v24
	v_div_scale_f32 v25, vcc, 1.0, v22, 1.0
	v_fma_f32 v30, -v24, v28, 1.0
	v_fmac_f32_e32 v28, v30, v28
	v_mul_f32_e32 v30, v25, v28
	v_fma_f32 v32, -v24, v30, v25
	v_fmac_f32_e32 v30, v32, v28
	v_fma_f32 v24, -v24, v30, v25
	v_div_fmas_f32 v24, v24, v28, v30
	v_div_fixup_f32 v22, v24, v22, 1.0
	v_pk_mul_f32 v[24:25], v[22:23], v[50:51] op_sel_hi:[0,1]
	v_pk_mul_f32 v[50:51], v[22:23], v[52:53] op_sel_hi:[0,1]
	v_pk_mul_f32 v[2:3], v[50:51], v[132:133]
	v_pk_mul_f32 v[0:1], v[24:25], v[130:131]
	global_store_dwordx4 v[20:21], v[0:3], off offset:-4096
	s_nop 1
	v_pk_mul_f32 v[24:25], v[22:23], v[34:35] op_sel_hi:[0,1]
	v_pk_mul_f32 v[34:35], v[22:23], v[54:55] op_sel_hi:[0,1]
	v_mov_b32_e32 v30, v33
	v_mov_b32_e32 v28, v23
	v_pk_mul_f32 v[0:1], v[34:35], v[134:135]
	v_pk_mul_f32 v[2:3], v[24:25], v[136:137]
	global_store_dwordx4 v[20:21], v[0:3], off offset:-3072
	s_nop 1
	v_mov_b32_e32 v24, v40
	v_mov_b32_e32 v25, v42
	v_mov_b32_e32 v42, v41
	v_pk_mul_f32 v[24:25], v[22:23], v[24:25] op_sel_hi:[0,1]
	v_pk_mul_f32 v[34:35], v[22:23], v[42:43] op_sel_hi:[0,1]
	v_pk_mul_f32 v[0:1], v[24:25], v[138:139]
	v_pk_mul_f32 v[2:3], v[34:35], v[140:141]
	global_store_dwordx4 v[20:21], v[0:3], off offset:-2048
	s_nop 1
	v_mov_b32_e32 v24, v44
	v_mov_b32_e32 v25, v46
	v_mov_b32_e32 v46, v45
	v_pk_mul_f32 v[24:25], v[22:23], v[24:25] op_sel_hi:[0,1]
	v_pk_mul_f32 v[34:35], v[22:23], v[46:47] op_sel_hi:[0,1]
	v_pk_mul_f32 v[0:1], v[24:25], v[142:143]
	v_pk_mul_f32 v[2:3], v[34:35], v[144:145]
	global_store_dwordx4 v[20:21], v[0:3], off offset:-1024
	s_nop 1
	v_pk_mul_f32 v[24:25], v[22:23], v[48:49] op_sel_hi:[0,1]
	v_pk_mul_f32 v[34:35], v[22:23], v[62:63] op_sel_hi:[0,1]
	v_pk_mul_f32 v[0:1], v[34:35], v[146:147]
	v_pk_mul_f32 v[2:3], v[24:25], v[148:149]
	global_store_dwordx4 v[20:21], v[0:3], off
	s_nop 1
	v_pk_mul_f32 v[24:25], v[22:23], v[26:27] op_sel_hi:[0,1]
	v_pk_mul_f32 v[26:27], v[22:23], v[72:73] op_sel_hi:[0,1]
	v_pk_mul_f32 v[0:1], v[26:27], v[150:151]
	v_pk_mul_f32 v[2:3], v[24:25], v[152:153]
	global_store_dwordx4 v[20:21], v[0:3], off offset:1024
	s_nop 1
	v_pk_mul_f32 v[24:25], v[22:23], v[38:39] op_sel_hi:[0,1]
	v_pk_mul_f32 v[26:27], v[22:23], v[36:37] op_sel_hi:[0,1]
	v_pk_mul_f32 v[0:1], v[26:27], v[154:155]
	v_pk_mul_f32 v[2:3], v[24:25], v[156:157]
	global_store_dwordx4 v[20:21], v[0:3], off offset:2048
	s_nop 1
	v_pk_mul_f32 v[24:25], v[22:23], v[28:29] op_sel_hi:[0,1]
	v_pk_mul_f32 v[22:23], v[22:23], v[30:31] op_sel_hi:[0,1]
	v_pk_mul_f32 v[0:1], v[24:25], v[158:159]
	v_pk_mul_f32 v[2:3], v[22:23], v[160:161]
	global_store_dwordx4 v[20:21], v[0:3], off offset:3072
	s_nop 1
	v_lshl_add_u64 v[20:21], v[20:21], 0, s[8:9]
	s_cbranch_scc1 .LBB0_4628
